# P4: the leftover attention q-blocks go to workgroups with a single hg_scan pass; background weight conversion waits per tile (counted vmcnt) instead of draining its 5-deep pipeline every 5 tiles
# speedup vs baseline: 1.0404x; 1.0069x over previous
.LBB0_203:
	s_mov_b32 s98, 0
	s_lshl_b32 s25, s21, 2
	v_lshrrev_b32_e32 v133, 3, v0
	v_lshlrev_b32_e32 v132, 4, v0
	v_mul_u32_u24_e32 v134, 0x84, v133
	v_lshlrev_b32_e32 v168, 11, v133
	v_or_b32_e32 v133, 0x200, v0
	s_add_u32 s34, s76, 0x224e8000
	v_lshlrev_b32_e32 v1, 2, v1
	v_and_b32_e32 v166, 0x70, v132
	v_lshrrev_b32_e32 v133, 3, v133
	s_addc_u32 s35, s77, 0
	v_lshlrev_b32_e32 v162, 2, v130
	v_mov_b32_e32 v165, 0
	v_add_u32_e32 v131, 0, v1
	v_add_u32_e32 v132, 0, v166
	v_mul_u32_u24_e32 v130, 0x210, v130
	v_mul_u32_u24_e32 v135, 0x84, v133
	s_waitcnt lgkmcnt(0)
	s_add_u32 s42, s76, 0x24e8000
	v_or_b32_e32 v163, 1, v1
	v_or_b32_e32 v172, 2, v1
	v_or_b32_e32 v173, 3, v1
	v_or_b32_e32 v174, 64, v1
	v_or_b32_e32 v175, 0x41, v1
	v_or_b32_e32 v176, 0x42, v1
	v_or_b32_e32 v177, 0x43, v1
	s_mov_b32 s13, 0
	v_mov_b32_e32 v167, v165
	v_mov_b32_e32 v169, v165
	v_lshlrev_b32_e32 v170, 11, v133
	v_mov_b32_e32 v171, v165
	s_addc_u32 s43, s77, 0
	s_mul_i32 s54, s21, 5
	s_mul_i32 s55, s21, 0x280
	s_lshl_b32 s56, s2, 7
	s_mul_i32 s57, s21, 6
	s_mul_i32 s58, s21, 0x300
	s_mul_i32 s59, s21, 7
	s_mul_i32 s60, s21, 0x380
	s_lshl_b32 s61, s21, 3
	s_lshl_b32 s64, s21, 10
	s_lshl_b32 s65, s21, 9
	v_add_u32_e32 v178, v131, v130
	v_add_u32_e32 v179, v132, v134
	v_add_u32_e32 v180, v132, v135
	s_mov_b32 s66, s2
	s_branch .LBB0_207
.LBB0_204:
	v_lshlrev_b32_e32 v164, 2, v162
	v_mul_u32_u24_e32 v98, s18, v1
	v_lshl_add_u64 v[122:123], s[16:17], 0, v[164:165]
	v_lshlrev_b32_e32 v164, 2, v98
	v_mul_u32_u24_e32 v100, s18, v163
	v_lshl_add_u64 v[98:99], v[122:123], 0, v[164:165]
	v_lshlrev_b32_e32 v164, 2, v100
	v_mul_u32_u24_e32 v106, s18, v172
	v_lshl_add_u64 v[102:103], v[122:123], 0, v[164:165]
	v_lshlrev_b32_e32 v164, 2, v106
	v_mul_u32_u24_e32 v108, s18, v173
	v_lshl_add_u64 v[106:107], v[122:123], 0, v[164:165]
	v_lshlrev_b32_e32 v164, 2, v108
	v_mul_u32_u24_e32 v114, s18, v174
	v_lshl_add_u64 v[110:111], v[122:123], 0, v[164:165]
	v_lshlrev_b32_e32 v164, 2, v114
	v_mul_u32_u24_e32 v116, s18, v175
	v_lshl_add_u64 v[114:115], v[122:123], 0, v[164:165]
	v_lshlrev_b32_e32 v164, 2, v116
	v_mul_u32_u24_e32 v124, s18, v176
	v_lshl_add_u64 v[118:119], v[122:123], 0, v[164:165]
	v_lshlrev_b32_e32 v164, 2, v124
	v_mul_u32_u24_e32 v126, s18, v177
	v_lshl_add_u64 v[124:125], v[122:123], 0, v[164:165]
	v_lshlrev_b32_e32 v164, 2, v126
	v_lshl_add_u64 v[126:127], v[122:123], 0, v[164:165]
	global_load_dwordx4 v[98:101], v[98:99], off nt
	s_nop 0
	global_load_dwordx4 v[102:105], v[102:103], off nt
	s_nop 0
	global_load_dwordx4 v[106:109], v[106:107], off nt
	s_nop 0
	global_load_dwordx4 v[110:113], v[110:111], off nt
	s_nop 0
	global_load_dwordx4 v[114:117], v[114:115], off nt
	s_nop 0
	global_load_dwordx4 v[118:121], v[118:119], off nt
	s_nop 0
	global_load_dwordx4 v[122:125], v[124:125], off nt
	s_nop 0
	global_load_dwordx4 v[126:129], v[126:127], off nt
	s_waitcnt vmcnt(40)
	s_mov_b32 s98, 1
	s_branch .Lc8_go_5
.LBB0_205:
	s_waitcnt vmcnt(0)
.Lc8_go_5:
	v_mul_f32_e32 v164, 0x42800000, v134
	v_mul_f32_e32 v181, 0x42800000, v130
	v_mov_b32_e32 v184, v165
	v_cvt_pk_fp8_f32 v184, v164, v181
	v_mul_f32_e32 v164, 0x42800000, v135
	v_mul_f32_e32 v181, 0x42800000, v131
	v_mov_b32_e32 v185, v165
	v_cvt_pk_fp8_f32 v185, v164, v181
	v_mul_f32_e32 v164, 0x42800000, v143
	v_mul_f32_e32 v181, 0x42800000, v139
	v_mov_b32_e32 v186, v165
	v_cvt_pk_fp8_f32 v185, v164, v181 op_sel:[0,0,1]
	v_mul_f32_e32 v164, 0x42800000, v136
	v_mul_f32_e32 v181, 0x42800000, v132
	v_cvt_pk_fp8_f32 v186, v164, v181
	v_mul_f32_e32 v164, 0x42800000, v137
	v_mul_f32_e32 v181, 0x42800000, v133
	v_mov_b32_e32 v187, v165
	v_cvt_pk_fp8_f32 v187, v164, v181
	v_mul_f32_e32 v164, 0x42800000, v145
	v_mul_f32_e32 v181, 0x42800000, v141
	v_mov_b32_e32 v188, v165
	v_cvt_pk_fp8_f32 v187, v164, v181 op_sel:[0,0,1]
	v_mul_f32_e32 v164, 0x42800000, v150
	v_mul_f32_e32 v181, 0x42800000, v146
	v_cvt_pk_fp8_f32 v188, v164, v181
	v_mul_f32_e32 v164, 0x42800000, v151
	v_mul_f32_e32 v181, 0x42800000, v147
	v_mov_b32_e32 v189, v165
	v_cvt_pk_fp8_f32 v189, v164, v181
	v_mul_f32_e32 v164, 0x42800000, v159
	v_mul_f32_e32 v181, 0x42800000, v155
	v_mul_f32_e32 v182, 0x42800000, v142
	v_mul_f32_e32 v183, 0x42800000, v138
	v_cvt_pk_fp8_f32 v189, v164, v181 op_sel:[0,0,1]
	v_mul_f32_e32 v164, 0x42800000, v152
	v_mul_f32_e32 v181, 0x42800000, v148
	v_mov_b32_e32 v192, v165
	v_cvt_pk_fp8_f32 v184, v182, v183 op_sel:[0,0,1]
	v_mul_f32_e32 v182, 0x42800000, v144
	v_mul_f32_e32 v183, 0x42800000, v140
	v_cvt_pk_fp8_f32 v192, v164, v181
	v_mul_f32_e32 v164, 0x42800000, v153
	v_mul_f32_e32 v181, 0x42800000, v149
	v_mov_b32_e32 v193, v165
	v_cvt_pk_fp8_f32 v186, v182, v183 op_sel:[0,0,1]
	v_mul_f32_e32 v182, 0x42800000, v158
	v_mul_f32_e32 v183, 0x42800000, v154
	v_cvt_pk_fp8_f32 v193, v164, v181
	v_cvt_pk_fp8_f32 v188, v182, v183 op_sel:[0,0,1]
	v_mul_f32_e32 v182, 0x42800000, v160
	v_mul_f32_e32 v183, 0x42800000, v156
	v_cvt_pk_fp8_f32 v192, v182, v183 op_sel:[0,0,1]
	v_mul_f32_e32 v164, 0x42800000, v161
	v_mul_f32_e32 v181, 0x42800000, v157
	s_add_i32 s12, s68, s21
	v_cvt_pk_fp8_f32 v193, v164, v181 op_sel:[0,0,1]
	s_add_i32 s12, s12, s21
	ds_write2_b32 v178, v184, v188 offset1:16
	ds_write2_b32 v178, v185, v189 offset0:33 offset1:49
	ds_write2_b32 v178, v186, v192 offset0:66 offset1:82
	ds_write2_b32 v178, v187, v193 offset0:99 offset1:115
	s_waitcnt lgkmcnt(0)
	s_barrier
	ds_read2_b32 v[182:183], v179 offset1:1
	ds_read2_b32 v[184:185], v179 offset0:2 offset1:3
	ds_read2_b32 v[186:187], v180 offset1:1
	ds_read2_b32 v[188:189], v180 offset0:2 offset1:3
	s_add_i32 s12, s12, s21
	v_lshl_add_u64 v[192:193], s[14:15], 0, v[166:167]
	s_add_i32 s66, s12, s21
	s_add_i32 s56, s56, s55
	v_lshl_add_u64 v[194:195], v[192:193], 0, v[168:169]
	s_cmpk_gt_i32 s66, 0x5fff
	s_waitcnt lgkmcnt(2)
	global_store_dwordx4 v[194:195], v[182:185], off nt
	s_cselect_b64 s[16:17], -1, 0
	s_nop 0
	v_lshl_add_u64 v[182:183], v[192:193], 0, v[170:171]
	s_waitcnt lgkmcnt(0)
	global_store_dwordx4 v[182:183], v[186:189], off nt
	s_barrier

.LBB0_212:
	v_lshlrev_b32_e32 v164, 2, v162
	v_mul_u32_u24_e32 v130, s18, v1
	v_lshl_add_u64 v[154:155], s[16:17], 0, v[164:165]
	v_lshlrev_b32_e32 v164, 2, v130
	v_mul_u32_u24_e32 v132, s18, v163
	v_lshl_add_u64 v[130:131], v[154:155], 0, v[164:165]
	v_lshlrev_b32_e32 v164, 2, v132
	v_mul_u32_u24_e32 v138, s18, v172
	v_lshl_add_u64 v[132:133], v[154:155], 0, v[164:165]
	v_lshlrev_b32_e32 v164, 2, v138
	v_mul_u32_u24_e32 v140, s18, v173
	v_lshl_add_u64 v[138:139], v[154:155], 0, v[164:165]
	v_lshlrev_b32_e32 v164, 2, v140
	v_mul_u32_u24_e32 v146, s18, v174
	v_lshl_add_u64 v[140:141], v[154:155], 0, v[164:165]
	v_lshlrev_b32_e32 v164, 2, v146
	v_mul_u32_u24_e32 v148, s18, v175
	v_lshl_add_u64 v[146:147], v[154:155], 0, v[164:165]
	v_lshlrev_b32_e32 v164, 2, v148
	v_mul_u32_u24_e32 v156, s18, v176
	v_lshl_add_u64 v[148:149], v[154:155], 0, v[164:165]
	v_lshlrev_b32_e32 v164, 2, v156
	v_mul_u32_u24_e32 v158, s18, v177
	v_lshl_add_u64 v[156:157], v[154:155], 0, v[164:165]
	v_lshlrev_b32_e32 v164, 2, v158
	v_lshl_add_u64 v[154:155], v[154:155], 0, v[164:165]
	global_load_dwordx4 v[134:137], v[130:131], off nt
	s_nop 0
	global_load_dwordx4 v[130:133], v[132:133], off nt
	s_nop 0
	global_load_dwordx4 v[142:145], v[138:139], off nt
	s_nop 0
	global_load_dwordx4 v[138:141], v[140:141], off nt
	s_nop 0
	global_load_dwordx4 v[150:153], v[146:147], off nt
	s_nop 0
	global_load_dwordx4 v[146:149], v[148:149], off nt
	s_nop 0
	global_load_dwordx4 v[158:161], v[156:157], off nt
	s_nop 0
	global_load_dwordx4 v[154:157], v[154:155], off nt
	s_cmp_eq_u32 s98, 0
	s_cbranch_scc1 .Lc8_f_1
	s_waitcnt vmcnt(40)
	s_branch .Lc8_go_1
.Lc8_f_1:
	s_waitcnt vmcnt(32)
	s_branch .Lc8_go_1

.Lc8_go_1:
	v_mul_f32_e32 v164, 0x42800000, v6
	v_mul_f32_e32 v181, 0x42800000, v2
	v_mov_b32_e32 v184, v165
	v_cvt_pk_fp8_f32 v184, v164, v181
	v_mul_f32_e32 v164, 0x42800000, v7
	v_mul_f32_e32 v181, 0x42800000, v3
	v_mov_b32_e32 v185, v165
	v_cvt_pk_fp8_f32 v185, v164, v181
	v_mul_f32_e32 v164, 0x42800000, v15
	v_mul_f32_e32 v181, 0x42800000, v11
	v_mov_b32_e32 v186, v165
	v_cvt_pk_fp8_f32 v185, v164, v181 op_sel:[0,0,1]
	v_mul_f32_e32 v164, 0x42800000, v8
	v_mul_f32_e32 v181, 0x42800000, v4
	v_cvt_pk_fp8_f32 v186, v164, v181
	v_mul_f32_e32 v164, 0x42800000, v9
	v_mul_f32_e32 v181, 0x42800000, v5
	v_mov_b32_e32 v187, v165
	v_cvt_pk_fp8_f32 v187, v164, v181
	v_mul_f32_e32 v164, 0x42800000, v17
	v_mul_f32_e32 v181, 0x42800000, v13
	v_mov_b32_e32 v188, v165
	v_cvt_pk_fp8_f32 v187, v164, v181 op_sel:[0,0,1]
	v_mul_f32_e32 v164, 0x42800000, v22
	v_mul_f32_e32 v181, 0x42800000, v18
	v_cvt_pk_fp8_f32 v188, v164, v181
	v_mul_f32_e32 v164, 0x42800000, v23
	v_mul_f32_e32 v181, 0x42800000, v19
	v_mov_b32_e32 v189, v165
	v_cvt_pk_fp8_f32 v189, v164, v181
	v_mul_f32_e32 v164, 0x42800000, v31
	v_mul_f32_e32 v181, 0x42800000, v27
	v_mul_f32_e32 v182, 0x42800000, v14
	v_mul_f32_e32 v183, 0x42800000, v10
	v_cvt_pk_fp8_f32 v189, v164, v181 op_sel:[0,0,1]
	v_mul_f32_e32 v164, 0x42800000, v24
	v_mul_f32_e32 v181, 0x42800000, v20
	v_mov_b32_e32 v192, v165
	v_cvt_pk_fp8_f32 v184, v182, v183 op_sel:[0,0,1]
	v_mul_f32_e32 v182, 0x42800000, v16
	v_mul_f32_e32 v183, 0x42800000, v12
	v_cvt_pk_fp8_f32 v192, v164, v181
	v_mul_f32_e32 v164, 0x42800000, v25
	v_mul_f32_e32 v181, 0x42800000, v21
	v_mov_b32_e32 v193, v165
	v_cvt_pk_fp8_f32 v186, v182, v183 op_sel:[0,0,1]
	v_mul_f32_e32 v182, 0x42800000, v30
	v_mul_f32_e32 v183, 0x42800000, v26
	v_cvt_pk_fp8_f32 v193, v164, v181
	v_cvt_pk_fp8_f32 v188, v182, v183 op_sel:[0,0,1]
	v_mul_f32_e32 v182, 0x42800000, v32
	v_mul_f32_e32 v183, 0x42800000, v28
	v_cvt_pk_fp8_f32 v192, v182, v183 op_sel:[0,0,1]
	v_mul_f32_e32 v164, 0x42800000, v33
	v_mul_f32_e32 v181, 0x42800000, v29
	v_cvt_pk_fp8_f32 v193, v164, v181 op_sel:[0,0,1]
	ds_write2_b32 v178, v184, v188 offset1:16
	ds_write2_b32 v178, v185, v189 offset0:33 offset1:49
	ds_write2_b32 v178, v186, v192 offset0:66 offset1:82
	ds_write2_b32 v178, v187, v193 offset0:99 offset1:115
	s_waitcnt lgkmcnt(0)
	s_barrier
	ds_read2_b32 v[182:183], v179 offset1:1
	ds_read2_b32 v[184:185], v179 offset0:2 offset1:3
	ds_read2_b32 v[186:187], v180 offset1:1
	ds_read2_b32 v[188:189], v180 offset0:2 offset1:3
	v_lshl_add_u64 v[192:193], s[0:1], 0, v[166:167]
	v_lshl_add_u64 v[194:195], v[192:193], 0, v[168:169]
	s_add_i32 s68, s66, s21
	s_waitcnt lgkmcnt(2)
	global_store_dwordx4 v[194:195], v[182:185], off nt
	s_cmpk_gt_i32 s68, 0x5fff
	s_mov_b64 s[16:17], -1
	v_lshl_add_u64 v[182:183], v[192:193], 0, v[170:171]
	s_waitcnt lgkmcnt(0)
	global_store_dwordx4 v[182:183], v[186:189], off nt
	s_barrier
	s_cbranch_scc1 .LBB0_206
	s_add_i32 s69, s54, s66
	s_cmpk_gt_i32 s69, 0x5fff
	s_cbranch_scc1 .LBB0_220
	s_cmpk_gt_i32 s69, 0x3fff
	s_mov_b64 s[18:19], -1
	s_cbranch_scc0 .LBB0_217
	s_add_i32 s0, s69, 0xffffc000
	s_lshr_b32 s12, s0, 8
	s_bfe_u32 s18, s69, 0x40004
	s_lshl_b64 s[0:1], s[12:13], 24
	v_readlane_b32 s80, v254, 0
	v_readlane_b32 s81, v254, 1
	s_add_u32 s0, s80, s0
	s_addc_u32 s1, s81, s1
	s_lshl_b32 s16, s18, 20
	s_add_u32 s0, s0, s16
	s_addc_u32 s1, s1, 0
	s_add_i32 s16, s55, s56
	s_and_b32 s19, s16, 0x780
	s_lshl_b32 s16, s19, 2
	s_add_u32 s16, s0, s16
	s_addc_u32 s17, s1, 0
	s_lshl_b64 s[0:1], s[12:13], 22
	s_lshl_b32 s12, s19, 11
	s_add_u32 s0, s34, s0
	s_addc_u32 s1, s35, s1
	s_add_u32 s0, s0, s12
	s_addc_u32 s1, s1, 0
	s_lshl_b32 s12, s18, 7
	s_add_u32 s0, s0, s12
	v_readlane_b32 s82, v254, 2
	v_readlane_b32 s83, v254, 3
	v_readlane_b32 s84, v254, 4
	v_readlane_b32 s85, v254, 5
	v_readlane_b32 s86, v254, 6
	v_readlane_b32 s87, v254, 7
	s_addc_u32 s1, s1, 0
	s_mov_b64 s[18:19], 0

.LBB0_219:
	v_lshlrev_b32_e32 v164, 2, v162
	v_mul_u32_u24_e32 v2, s18, v1
	v_lshl_add_u64 v[26:27], s[16:17], 0, v[164:165]
	v_lshlrev_b32_e32 v164, 2, v2
	v_mul_u32_u24_e32 v4, s18, v163
	v_lshl_add_u64 v[2:3], v[26:27], 0, v[164:165]
	v_lshlrev_b32_e32 v164, 2, v4
	v_mul_u32_u24_e32 v10, s18, v172
	v_lshl_add_u64 v[4:5], v[26:27], 0, v[164:165]
	v_lshlrev_b32_e32 v164, 2, v10
	v_mul_u32_u24_e32 v12, s18, v173
	v_lshl_add_u64 v[10:11], v[26:27], 0, v[164:165]
	v_lshlrev_b32_e32 v164, 2, v12
	v_mul_u32_u24_e32 v18, s18, v174
	v_lshl_add_u64 v[12:13], v[26:27], 0, v[164:165]
	v_lshlrev_b32_e32 v164, 2, v18
	v_mul_u32_u24_e32 v20, s18, v175
	v_lshl_add_u64 v[18:19], v[26:27], 0, v[164:165]
	v_lshlrev_b32_e32 v164, 2, v20
	v_mul_u32_u24_e32 v28, s18, v176
	v_lshl_add_u64 v[20:21], v[26:27], 0, v[164:165]
	v_lshlrev_b32_e32 v164, 2, v28
	v_mul_u32_u24_e32 v30, s18, v177
	v_lshl_add_u64 v[28:29], v[26:27], 0, v[164:165]
	v_lshlrev_b32_e32 v164, 2, v30
	v_lshl_add_u64 v[26:27], v[26:27], 0, v[164:165]
	global_load_dwordx4 v[6:9], v[2:3], off nt
	s_nop 0
	global_load_dwordx4 v[2:5], v[4:5], off nt
	s_nop 0
	global_load_dwordx4 v[14:17], v[10:11], off nt
	s_nop 0
	global_load_dwordx4 v[10:13], v[12:13], off nt
	s_nop 0
	global_load_dwordx4 v[22:25], v[18:19], off nt
	s_nop 0
	global_load_dwordx4 v[18:21], v[20:21], off nt
	s_nop 0
	global_load_dwordx4 v[30:33], v[28:29], off nt
	s_nop 0
	global_load_dwordx4 v[26:29], v[26:27], off nt
	s_cmp_eq_u32 s98, 0
	s_cbranch_scc1 .Lc8_f_2
	s_waitcnt vmcnt(40)
	s_branch .Lc8_go_2

.LBB0_220:
	s_waitcnt vmcnt(0)
.Lc8_go_2:
	v_mul_f32_e32 v164, 0x42800000, v34
	v_mul_f32_e32 v181, 0x42800000, v38
	v_mov_b32_e32 v184, v165
	v_cvt_pk_fp8_f32 v184, v164, v181
	v_mul_f32_e32 v164, 0x42800000, v35
	v_mul_f32_e32 v181, 0x42800000, v39
	v_mov_b32_e32 v185, v165
	v_cvt_pk_fp8_f32 v185, v164, v181
	v_mul_f32_e32 v164, 0x42800000, v43
	v_mul_f32_e32 v181, 0x42800000, v47
	v_mov_b32_e32 v186, v165
	v_cvt_pk_fp8_f32 v185, v164, v181 op_sel:[0,0,1]
	v_mul_f32_e32 v164, 0x42800000, v36
	v_mul_f32_e32 v181, 0x42800000, v40
	v_cvt_pk_fp8_f32 v186, v164, v181
	v_mul_f32_e32 v164, 0x42800000, v37
	v_mul_f32_e32 v181, 0x42800000, v41
	v_mov_b32_e32 v187, v165
	v_cvt_pk_fp8_f32 v187, v164, v181
	v_mul_f32_e32 v164, 0x42800000, v45
	v_mul_f32_e32 v181, 0x42800000, v49
	v_mov_b32_e32 v188, v165
	v_cvt_pk_fp8_f32 v187, v164, v181 op_sel:[0,0,1]
	v_mul_f32_e32 v164, 0x42800000, v50
	v_mul_f32_e32 v181, 0x42800000, v54
	v_cvt_pk_fp8_f32 v188, v164, v181
	v_mul_f32_e32 v164, 0x42800000, v51
	v_mul_f32_e32 v181, 0x42800000, v55
	v_mov_b32_e32 v189, v165
	v_cvt_pk_fp8_f32 v189, v164, v181
	v_mul_f32_e32 v164, 0x42800000, v59
	v_mul_f32_e32 v181, 0x42800000, v63
	v_mul_f32_e32 v182, 0x42800000, v42
	v_mul_f32_e32 v183, 0x42800000, v46
	v_cvt_pk_fp8_f32 v189, v164, v181 op_sel:[0,0,1]
	v_mul_f32_e32 v164, 0x42800000, v52
	v_mul_f32_e32 v181, 0x42800000, v56
	v_mov_b32_e32 v192, v165
	v_cvt_pk_fp8_f32 v184, v182, v183 op_sel:[0,0,1]
	v_mul_f32_e32 v182, 0x42800000, v44
	v_mul_f32_e32 v183, 0x42800000, v48
	v_cvt_pk_fp8_f32 v192, v164, v181
	v_mul_f32_e32 v164, 0x42800000, v53
	v_mul_f32_e32 v181, 0x42800000, v57
	v_mov_b32_e32 v193, v165
	v_cvt_pk_fp8_f32 v186, v182, v183 op_sel:[0,0,1]
	v_mul_f32_e32 v182, 0x42800000, v58
	v_mul_f32_e32 v183, 0x42800000, v62
	v_cvt_pk_fp8_f32 v193, v164, v181
	v_cvt_pk_fp8_f32 v188, v182, v183 op_sel:[0,0,1]
	v_mul_f32_e32 v182, 0x42800000, v60
	v_mul_f32_e32 v183, 0x42800000, v64
	v_cvt_pk_fp8_f32 v192, v182, v183 op_sel:[0,0,1]
	v_mul_f32_e32 v164, 0x42800000, v61
	v_mul_f32_e32 v181, 0x42800000, v65
	v_cvt_pk_fp8_f32 v193, v164, v181 op_sel:[0,0,1]
	ds_write2_b32 v178, v184, v188 offset1:16
	ds_write2_b32 v178, v185, v189 offset0:33 offset1:49
	ds_write2_b32 v178, v186, v192 offset0:66 offset1:82
	ds_write2_b32 v178, v187, v193 offset0:99 offset1:115
	s_waitcnt lgkmcnt(0)
	s_barrier
	ds_read2_b32 v[182:183], v179 offset1:1
	ds_read2_b32 v[184:185], v179 offset0:2 offset1:3
	ds_read2_b32 v[186:187], v180 offset1:1
	ds_read2_b32 v[188:189], v180 offset0:2 offset1:3
	v_lshl_add_u64 v[192:193], s[6:7], 0, v[166:167]
	v_lshl_add_u64 v[194:195], v[192:193], 0, v[168:169]
	s_add_i32 s12, s22, s66
	s_waitcnt lgkmcnt(2)
	global_store_dwordx4 v[194:195], v[182:185], off nt
	s_cmpk_gt_i32 s12, 0x5fff
	s_mov_b64 s[16:17], -1
	v_lshl_add_u64 v[182:183], v[192:193], 0, v[170:171]
	s_waitcnt lgkmcnt(0)
	global_store_dwordx4 v[182:183], v[186:189], off nt
	s_barrier
	s_cbranch_scc1 .LBB0_206
	s_add_i32 s69, s57, s66
	s_cmpk_gt_i32 s69, 0x5fff
	s_cbranch_scc1 .LBB0_227
	s_cmpk_gt_i32 s69, 0x3fff
	s_mov_b64 s[18:19], -1
	s_cbranch_scc0 .LBB0_224
	s_add_i32 s6, s69, 0xffffc000
	s_lshr_b32 s12, s6, 8
	s_bfe_u32 s18, s69, 0x40004
	s_lshl_b64 s[6:7], s[12:13], 24
	v_readlane_b32 s80, v254, 0
	v_readlane_b32 s81, v254, 1
	s_add_u32 s6, s80, s6
	s_addc_u32 s7, s81, s7
	s_lshl_b32 s16, s18, 20
	s_add_u32 s6, s6, s16
	s_addc_u32 s7, s7, 0
	s_add_i32 s16, s58, s56
	s_and_b32 s19, s16, 0x780
	s_lshl_b32 s16, s19, 2
	s_add_u32 s16, s6, s16
	s_addc_u32 s17, s7, 0
	s_lshl_b64 s[6:7], s[12:13], 22
	s_lshl_b32 s12, s19, 11
	s_add_u32 s6, s34, s6
	s_addc_u32 s7, s35, s7
	s_add_u32 s6, s6, s12
	s_addc_u32 s7, s7, 0
	s_lshl_b32 s12, s18, 7
	s_add_u32 s6, s6, s12
	v_readlane_b32 s82, v254, 2
	v_readlane_b32 s83, v254, 3
	v_readlane_b32 s84, v254, 4
	v_readlane_b32 s85, v254, 5
	v_readlane_b32 s86, v254, 6
	v_readlane_b32 s87, v254, 7
	s_addc_u32 s7, s7, 0
	s_mov_b64 s[18:19], 0

.LBB0_226:
	v_lshlrev_b32_e32 v164, 2, v162
	v_mul_u32_u24_e32 v34, s18, v1
	v_lshl_add_u64 v[58:59], s[16:17], 0, v[164:165]
	v_lshlrev_b32_e32 v164, 2, v34
	v_mul_u32_u24_e32 v36, s18, v163
	v_lshl_add_u64 v[34:35], v[58:59], 0, v[164:165]
	v_lshlrev_b32_e32 v164, 2, v36
	v_mul_u32_u24_e32 v42, s18, v172
	v_lshl_add_u64 v[38:39], v[58:59], 0, v[164:165]
	v_lshlrev_b32_e32 v164, 2, v42
	v_mul_u32_u24_e32 v44, s18, v173
	v_lshl_add_u64 v[42:43], v[58:59], 0, v[164:165]
	v_lshlrev_b32_e32 v164, 2, v44
	v_mul_u32_u24_e32 v50, s18, v174
	v_lshl_add_u64 v[46:47], v[58:59], 0, v[164:165]
	v_lshlrev_b32_e32 v164, 2, v50
	v_mul_u32_u24_e32 v52, s18, v175
	v_lshl_add_u64 v[50:51], v[58:59], 0, v[164:165]
	v_lshlrev_b32_e32 v164, 2, v52
	v_mul_u32_u24_e32 v60, s18, v176
	v_lshl_add_u64 v[54:55], v[58:59], 0, v[164:165]
	v_lshlrev_b32_e32 v164, 2, v60
	v_mul_u32_u24_e32 v62, s18, v177
	v_lshl_add_u64 v[60:61], v[58:59], 0, v[164:165]
	v_lshlrev_b32_e32 v164, 2, v62
	v_lshl_add_u64 v[62:63], v[58:59], 0, v[164:165]
	global_load_dwordx4 v[34:37], v[34:35], off nt
	s_nop 0
	global_load_dwordx4 v[38:41], v[38:39], off nt
	s_nop 0
	global_load_dwordx4 v[42:45], v[42:43], off nt
	s_nop 0
	global_load_dwordx4 v[46:49], v[46:47], off nt
	s_nop 0
	global_load_dwordx4 v[50:53], v[50:51], off nt
	s_nop 0
	global_load_dwordx4 v[54:57], v[54:55], off nt
	s_nop 0
	global_load_dwordx4 v[58:61], v[60:61], off nt
	s_nop 0
	global_load_dwordx4 v[62:65], v[62:63], off nt
	s_cmp_eq_u32 s98, 0
	s_cbranch_scc1 .Lc8_f_3
	s_waitcnt vmcnt(40)
	s_branch .Lc8_go_3

.LBB0_227:
	s_waitcnt vmcnt(0)
.Lc8_go_3:
	v_mul_f32_e32 v164, 0x42800000, v66
	v_mul_f32_e32 v181, 0x42800000, v70
	v_mov_b32_e32 v184, v165
	v_cvt_pk_fp8_f32 v184, v164, v181
	v_mul_f32_e32 v164, 0x42800000, v67
	v_mul_f32_e32 v181, 0x42800000, v71
	v_mov_b32_e32 v185, v165
	v_cvt_pk_fp8_f32 v185, v164, v181
	v_mul_f32_e32 v164, 0x42800000, v75
	v_mul_f32_e32 v181, 0x42800000, v79
	v_mov_b32_e32 v186, v165
	v_cvt_pk_fp8_f32 v185, v164, v181 op_sel:[0,0,1]
	v_mul_f32_e32 v164, 0x42800000, v68
	v_mul_f32_e32 v181, 0x42800000, v72
	v_cvt_pk_fp8_f32 v186, v164, v181
	v_mul_f32_e32 v164, 0x42800000, v69
	v_mul_f32_e32 v181, 0x42800000, v73
	v_mov_b32_e32 v187, v165
	v_cvt_pk_fp8_f32 v187, v164, v181
	v_mul_f32_e32 v164, 0x42800000, v77
	v_mul_f32_e32 v181, 0x42800000, v81
	v_mov_b32_e32 v188, v165
	v_cvt_pk_fp8_f32 v187, v164, v181 op_sel:[0,0,1]
	v_mul_f32_e32 v164, 0x42800000, v82
	v_mul_f32_e32 v181, 0x42800000, v86
	v_cvt_pk_fp8_f32 v188, v164, v181
	v_mul_f32_e32 v164, 0x42800000, v83
	v_mul_f32_e32 v181, 0x42800000, v87
	v_mov_b32_e32 v189, v165
	v_cvt_pk_fp8_f32 v189, v164, v181
	v_mul_f32_e32 v164, 0x42800000, v91
	v_mul_f32_e32 v181, 0x42800000, v95
	v_mul_f32_e32 v182, 0x42800000, v74
	v_mul_f32_e32 v183, 0x42800000, v78
	v_cvt_pk_fp8_f32 v189, v164, v181 op_sel:[0,0,1]
	v_mul_f32_e32 v164, 0x42800000, v84
	v_mul_f32_e32 v181, 0x42800000, v88
	v_mov_b32_e32 v192, v165
	v_cvt_pk_fp8_f32 v184, v182, v183 op_sel:[0,0,1]
	v_mul_f32_e32 v182, 0x42800000, v76
	v_mul_f32_e32 v183, 0x42800000, v80
	v_cvt_pk_fp8_f32 v192, v164, v181
	v_mul_f32_e32 v164, 0x42800000, v85
	v_mul_f32_e32 v181, 0x42800000, v89
	v_mov_b32_e32 v193, v165
	v_cvt_pk_fp8_f32 v186, v182, v183 op_sel:[0,0,1]
	v_mul_f32_e32 v182, 0x42800000, v90
	v_mul_f32_e32 v183, 0x42800000, v94
	v_cvt_pk_fp8_f32 v193, v164, v181
	v_cvt_pk_fp8_f32 v188, v182, v183 op_sel:[0,0,1]
	v_mul_f32_e32 v182, 0x42800000, v92
	v_mul_f32_e32 v183, 0x42800000, v96
	v_cvt_pk_fp8_f32 v192, v182, v183 op_sel:[0,0,1]
	v_mul_f32_e32 v164, 0x42800000, v93
	v_mul_f32_e32 v181, 0x42800000, v97
	v_cvt_pk_fp8_f32 v193, v164, v181 op_sel:[0,0,1]
	ds_write2_b32 v178, v184, v188 offset1:16
	ds_write2_b32 v178, v185, v189 offset0:33 offset1:49
	ds_write2_b32 v178, v186, v192 offset0:66 offset1:82
	ds_write2_b32 v178, v187, v193 offset0:99 offset1:115
	s_waitcnt lgkmcnt(0)
	s_barrier
	ds_read2_b32 v[182:183], v179 offset1:1
	ds_read2_b32 v[184:185], v179 offset0:2 offset1:3
	ds_read2_b32 v[186:187], v180 offset1:1
	ds_read2_b32 v[188:189], v180 offset0:2 offset1:3
	v_lshl_add_u64 v[192:193], s[8:9], 0, v[166:167]
	v_lshl_add_u64 v[194:195], v[192:193], 0, v[168:169]
	s_add_i32 s12, s23, s66
	s_waitcnt lgkmcnt(2)
	global_store_dwordx4 v[194:195], v[182:185], off nt
	s_cmpk_gt_i32 s12, 0x5fff
	s_mov_b64 s[16:17], -1
	v_lshl_add_u64 v[182:183], v[192:193], 0, v[170:171]
	s_waitcnt lgkmcnt(0)
	global_store_dwordx4 v[182:183], v[186:189], off nt
	s_barrier
	s_cbranch_scc1 .LBB0_206
	s_add_i32 s69, s59, s66
	s_cmpk_gt_i32 s69, 0x5fff
	s_cbranch_scc1 .LBB0_234
	s_cmpk_gt_i32 s69, 0x3fff
	s_mov_b64 s[18:19], -1
	s_cbranch_scc0 .LBB0_231
	s_add_i32 s8, s69, 0xffffc000
	s_lshr_b32 s12, s8, 8
	s_bfe_u32 s18, s69, 0x40004
	s_lshl_b64 s[8:9], s[12:13], 24
	v_readlane_b32 s80, v254, 0
	v_readlane_b32 s81, v254, 1
	s_add_u32 s8, s80, s8
	s_addc_u32 s9, s81, s9
	s_lshl_b32 s16, s18, 20
	s_add_u32 s8, s8, s16
	s_addc_u32 s9, s9, 0
	s_add_i32 s16, s60, s56
	s_and_b32 s19, s16, 0x780
	s_lshl_b32 s16, s19, 2
	s_add_u32 s16, s8, s16
	s_addc_u32 s17, s9, 0
	s_lshl_b64 s[8:9], s[12:13], 22
	s_lshl_b32 s12, s19, 11
	s_add_u32 s8, s34, s8
	s_addc_u32 s9, s35, s9
	s_add_u32 s8, s8, s12
	s_addc_u32 s9, s9, 0
	s_lshl_b32 s12, s18, 7
	s_add_u32 s8, s8, s12
	v_readlane_b32 s82, v254, 2
	v_readlane_b32 s83, v254, 3
	v_readlane_b32 s84, v254, 4
	v_readlane_b32 s85, v254, 5
	v_readlane_b32 s86, v254, 6
	v_readlane_b32 s87, v254, 7
	s_addc_u32 s9, s9, 0
	s_mov_b64 s[18:19], 0

.LBB0_233:
	v_lshlrev_b32_e32 v164, 2, v162
	v_mul_u32_u24_e32 v66, s18, v1
	v_lshl_add_u64 v[90:91], s[16:17], 0, v[164:165]
	v_lshlrev_b32_e32 v164, 2, v66
	v_mul_u32_u24_e32 v68, s18, v163
	v_lshl_add_u64 v[66:67], v[90:91], 0, v[164:165]
	v_lshlrev_b32_e32 v164, 2, v68
	v_mul_u32_u24_e32 v74, s18, v172
	v_lshl_add_u64 v[70:71], v[90:91], 0, v[164:165]
	v_lshlrev_b32_e32 v164, 2, v74
	v_mul_u32_u24_e32 v76, s18, v173
	v_lshl_add_u64 v[74:75], v[90:91], 0, v[164:165]
	v_lshlrev_b32_e32 v164, 2, v76
	v_mul_u32_u24_e32 v82, s18, v174
	v_lshl_add_u64 v[78:79], v[90:91], 0, v[164:165]
	v_lshlrev_b32_e32 v164, 2, v82
	v_mul_u32_u24_e32 v84, s18, v175
	v_lshl_add_u64 v[82:83], v[90:91], 0, v[164:165]
	v_lshlrev_b32_e32 v164, 2, v84
	v_mul_u32_u24_e32 v92, s18, v176
	v_lshl_add_u64 v[86:87], v[90:91], 0, v[164:165]
	v_lshlrev_b32_e32 v164, 2, v92
	v_mul_u32_u24_e32 v94, s18, v177
	v_lshl_add_u64 v[92:93], v[90:91], 0, v[164:165]
	v_lshlrev_b32_e32 v164, 2, v94
	v_lshl_add_u64 v[94:95], v[90:91], 0, v[164:165]
	global_load_dwordx4 v[66:69], v[66:67], off nt
	s_nop 0
	global_load_dwordx4 v[70:73], v[70:71], off nt
	s_nop 0
	global_load_dwordx4 v[74:77], v[74:75], off nt
	s_nop 0
	global_load_dwordx4 v[78:81], v[78:79], off nt
	s_nop 0
	global_load_dwordx4 v[82:85], v[82:83], off nt
	s_nop 0
	global_load_dwordx4 v[86:89], v[86:87], off nt
	s_nop 0
	global_load_dwordx4 v[90:93], v[92:93], off nt
	s_nop 0
	global_load_dwordx4 v[94:97], v[94:95], off nt
	s_cmp_eq_u32 s98, 0
	s_cbranch_scc1 .Lc8_f_4
	s_waitcnt vmcnt(40)
	s_branch .Lc8_go_4

.LBB0_234:
	s_waitcnt vmcnt(0)
.Lc8_go_4:
	v_mul_f32_e32 v164, 0x42800000, v98
	v_mul_f32_e32 v181, 0x42800000, v102
	v_mov_b32_e32 v184, v165
	v_cvt_pk_fp8_f32 v184, v164, v181
	v_mul_f32_e32 v164, 0x42800000, v99
	v_mul_f32_e32 v181, 0x42800000, v103
	v_mov_b32_e32 v185, v165
	v_cvt_pk_fp8_f32 v185, v164, v181
	v_mul_f32_e32 v164, 0x42800000, v107
	v_mul_f32_e32 v181, 0x42800000, v111
	v_mov_b32_e32 v186, v165
	v_cvt_pk_fp8_f32 v185, v164, v181 op_sel:[0,0,1]
	v_mul_f32_e32 v164, 0x42800000, v100
	v_mul_f32_e32 v181, 0x42800000, v104
	v_cvt_pk_fp8_f32 v186, v164, v181
	v_mul_f32_e32 v164, 0x42800000, v101
	v_mul_f32_e32 v181, 0x42800000, v105
	v_mov_b32_e32 v187, v165
	v_cvt_pk_fp8_f32 v187, v164, v181
	v_mul_f32_e32 v164, 0x42800000, v109
	v_mul_f32_e32 v181, 0x42800000, v113
	v_mov_b32_e32 v188, v165
	v_cvt_pk_fp8_f32 v187, v164, v181 op_sel:[0,0,1]
	v_mul_f32_e32 v164, 0x42800000, v114
	v_mul_f32_e32 v181, 0x42800000, v118
	v_cvt_pk_fp8_f32 v188, v164, v181
	v_mul_f32_e32 v164, 0x42800000, v115
	v_mul_f32_e32 v181, 0x42800000, v119
	v_mov_b32_e32 v189, v165
	v_cvt_pk_fp8_f32 v189, v164, v181
	v_mul_f32_e32 v164, 0x42800000, v123
	v_mul_f32_e32 v181, 0x42800000, v127
	v_mul_f32_e32 v182, 0x42800000, v106
	v_mul_f32_e32 v183, 0x42800000, v110
	v_cvt_pk_fp8_f32 v189, v164, v181 op_sel:[0,0,1]
	v_mul_f32_e32 v164, 0x42800000, v116
	v_mul_f32_e32 v181, 0x42800000, v120
	v_mov_b32_e32 v192, v165
	v_cvt_pk_fp8_f32 v184, v182, v183 op_sel:[0,0,1]
	v_mul_f32_e32 v182, 0x42800000, v108
	v_mul_f32_e32 v183, 0x42800000, v112
	v_cvt_pk_fp8_f32 v192, v164, v181
	v_mul_f32_e32 v164, 0x42800000, v117
	v_mul_f32_e32 v181, 0x42800000, v121
	v_mov_b32_e32 v193, v165
	v_cvt_pk_fp8_f32 v186, v182, v183 op_sel:[0,0,1]
	v_mul_f32_e32 v182, 0x42800000, v122
	v_mul_f32_e32 v183, 0x42800000, v126
	v_cvt_pk_fp8_f32 v193, v164, v181
	v_cvt_pk_fp8_f32 v188, v182, v183 op_sel:[0,0,1]
	v_mul_f32_e32 v182, 0x42800000, v124
	v_mul_f32_e32 v183, 0x42800000, v128
	v_cvt_pk_fp8_f32 v192, v182, v183 op_sel:[0,0,1]
	v_mul_f32_e32 v164, 0x42800000, v125
	v_mul_f32_e32 v181, 0x42800000, v129
	v_cvt_pk_fp8_f32 v193, v164, v181 op_sel:[0,0,1]
	ds_write2_b32 v178, v184, v188 offset1:16
	ds_write2_b32 v178, v185, v189 offset0:33 offset1:49
	ds_write2_b32 v178, v186, v192 offset0:66 offset1:82
	ds_write2_b32 v178, v187, v193 offset0:99 offset1:115
	s_waitcnt lgkmcnt(0)
	s_barrier
	ds_read2_b32 v[182:183], v179 offset1:1
	ds_read2_b32 v[184:185], v179 offset0:2 offset1:3
	ds_read2_b32 v[186:187], v180 offset1:1
	ds_read2_b32 v[188:189], v180 offset0:2 offset1:3
	v_lshl_add_u64 v[192:193], s[10:11], 0, v[166:167]
	v_lshl_add_u64 v[194:195], v[192:193], 0, v[168:169]
	s_waitcnt lgkmcnt(2)
	global_store_dwordx4 v[194:195], v[182:185], off nt
	s_cmpk_gt_i32 s67, 0x5fff
	s_mov_b64 s[16:17], -1
	v_lshl_add_u64 v[182:183], v[192:193], 0, v[170:171]
	s_waitcnt lgkmcnt(0)
	global_store_dwordx4 v[182:183], v[186:189], off nt
	s_barrier
	s_cbranch_scc1 .LBB0_206
	s_add_i32 s66, s61, s66
	s_cmpk_gt_i32 s66, 0x5fff
	s_cbranch_scc1 .LBB0_205
	s_cmpk_gt_i32 s66, 0x3fff
	s_mov_b64 s[18:19], -1
	s_cbranch_scc0 .LBB0_238
	s_add_i32 s10, s66, 0xffffc000
	s_lshr_b32 s12, s10, 8
	s_bfe_u32 s18, s66, 0x40004
	s_lshl_b64 s[10:11], s[12:13], 24
	v_readlane_b32 s80, v254, 0
	v_readlane_b32 s81, v254, 1
	s_add_u32 s10, s80, s10
	s_addc_u32 s11, s81, s11
	s_lshl_b32 s16, s18, 20
	s_add_u32 s10, s10, s16
	s_addc_u32 s11, s11, 0
	s_add_i32 s16, s64, s56
	s_and_b32 s19, s16, 0x780
	s_lshl_b32 s16, s19, 2
	s_add_u32 s16, s10, s16
	s_addc_u32 s17, s11, 0
	s_lshl_b64 s[10:11], s[12:13], 22
	s_lshl_b32 s12, s19, 11
	s_add_u32 s10, s34, s10
	s_addc_u32 s11, s35, s11
	s_add_u32 s10, s10, s12
	s_addc_u32 s11, s11, 0
	s_lshl_b32 s12, s18, 7
	s_add_u32 s10, s10, s12
	v_readlane_b32 s82, v254, 2
	v_readlane_b32 s83, v254, 3
	v_readlane_b32 s84, v254, 4
	v_readlane_b32 s85, v254, 5
	v_readlane_b32 s86, v254, 6
	v_readlane_b32 s87, v254, 7
	s_addc_u32 s11, s11, 0
	s_mov_b64 s[18:19], 0

.LBB0_403:
	s_or_b64 exec, exec, s[0:1]
	s_abs_i32 s0, s24
	v_cvt_f32_u32_e32 v1, s0
	s_sub_i32 s3, 0, s0
	s_ashr_i32 s1, s24, 31
	s_mov_b32 s25, 0
	v_rcp_iflag_f32_e32 v1, v1
	s_nop 0
	v_mul_f32_e32 v1, 0x4f7ffffe, v1
	v_cvt_u32_f32_e32 v1, v1
	s_nop 0
	v_readfirstlane_b32 s4, v1
	s_mul_i32 s3, s3, s4
	s_mul_hi_u32 s3, s4, s3
	s_add_i32 s4, s4, s3
	s_lshr_b32 s3, s4, 23
	s_mul_i32 s4, s3, s0
	s_sub_i32 s4, 0x200, s4
	s_add_i32 s5, s3, 1
	s_sub_i32 s6, s4, s0
	s_cmp_ge_u32 s4, s0
	s_cselect_b32 s3, s5, s3
	s_cselect_b32 s4, s6, s4
	s_add_i32 s5, s3, 1
	s_cmp_ge_u32 s4, s0
	s_cselect_b32 s0, s5, s3
	s_xor_b32 s0, s0, s1
	s_sub_i32 s0, s0, s1
	s_mul_i32 s5, s0, s24
	s_sub_i32 s4, 0x200, s5
	s_lshl_b32 s3, s0, 1
	s_lshl_b32 s0, s4, 1
	s_cmp_gt_i32 s0, s24
	s_cbranch_scc1 .LBB0_407
	s_mov_b32 s21, -1
	s_sub_i32 s98, 0x100, s24
	s_max_i32 s98, s98, 0
	s_sub_i32 s99, s24, s98
	s_cmp_lt_i32 s99, s0
	s_cselect_b32 s98, 0, s98
	s_sub_i32 s98, s20, s98
	s_cmp_ge_u32 s98, s0
	s_mov_b32 s23, s3
	s_cbranch_scc1 .LBB0_406
	s_ashr_i32 s0, s98, 1
	s_or_b32 s23, s3, 1
	s_add_i32 s21, s5, s0
	s_mov_b32 s25, s2
